# baseline (speedup 1.0000x reference)
.LBB0_39:
	s_or_b64 exec, exec, s[6:7]
	v_cvt_pk_f16_f32 v73, v118, v119
	v_cvt_pk_f16_f32 v72, v116, v117
	v_add_u32_e32 v76, v103, v105
	v_cvt_pk_f16_f32 v75, v122, v123
	v_cvt_pk_f16_f32 v74, v120, v121
	s_waitcnt lgkmcnt(0)
	s_barrier
	s_and_saveexec_b64 s[6:7], s[0:1]
	s_cbranch_execz .Lwos_nonworker
	v_mov_b32_e32 v215, 0
	v_add_u32_e32 v54, v224, v223
	ds_read_b128 v[34:37], v54
	s_movk_i32 s0, 0x110
	v_mad_u32_u24 v70, v220, s0, v223
	ds_read_b128 v[38:41], v70 offset:34816
	ds_read_b128 v[42:45], v54 offset:32
	ds_read_b128 v[46:49], v70 offset:34848
	v_lshl_or_b32 v32, v251, 12, v32
	v_add_u32_e32 v78, 0x18800, v32
	v_div_scale_f32 v82, s[0:1], s10, s10, 1.0
	v_rcp_f32_e32 v84, v82
	v_div_scale_f32 v83, vcc, 1.0, s10, 1.0
	s_waitcnt vmcnt(0) lgkmcnt(2)
	v_mfma_f32_32x32x16_f16 v[16:31], v[34:37], v[38:41], v[16:31]
	ds_read_b128 v[34:37], v54 offset:64
	ds_read_b128 v[38:41], v70 offset:34880
	s_waitcnt lgkmcnt(2)
	v_mfma_f32_32x32x16_f16 v[16:31], v[42:45], v[46:49], v[16:31]
	ds_read_b128 v[42:45], v54 offset:96
	ds_read_b128 v[46:49], v70 offset:34912
	s_waitcnt lgkmcnt(2)
	v_mfma_f32_32x32x16_f16 v[16:31], v[34:37], v[38:41], v[16:31]
	ds_read_b128 v[32:35], v54 offset:128
	ds_read_b128 v[36:39], v54 offset:160
	ds_read_b128 v[50:53], v54 offset:192
	ds_read_b128 v[54:57], v54 offset:224
	ds_read_b128 v[58:61], v70 offset:34944
	ds_read_b128 v[62:65], v70 offset:34976
	ds_read_b128 v[66:69], v70 offset:35008
	ds_read_b128 v[70:73], v70 offset:35040
	s_waitcnt lgkmcnt(8)
	v_mfma_f32_32x32x16_f16 v[16:31], v[42:45], v[46:49], v[16:31]
	ds_read_b128 v[40:43], v78
	ds_read_b128 v[44:47], v78 offset:1024
	ds_read_b128 v[74:77], v78 offset:2048
	ds_read_b128 v[78:81], v78 offset:3072
	v_add_u32_e32 v90, v103, v105
	v_cvt_pk_f16_f32 v87, v118, v119
	v_cvt_pk_f16_f32 v86, v116, v117
	v_cvt_pk_f16_f32 v89, v122, v123
	v_cvt_pk_f16_f32 v88, v120, v121
	ds_write2_b64 v90, v[86:87], v[88:89] offset1:34
	v_cvt_pk_f16_f32 v87, v126, v127
	v_cvt_pk_f16_f32 v86, v124, v125
	v_cvt_pk_f16_f32 v89, v130, v131
	v_cvt_pk_f16_f32 v88, v128, v129
	ds_write2_b64 v90, v[86:87], v[88:89] offset0:68 offset1:102
	v_cvt_pk_f16_f32 v87, v134, v135
	v_cvt_pk_f16_f32 v86, v132, v133
	v_cvt_pk_f16_f32 v89, v138, v139
	v_cvt_pk_f16_f32 v88, v136, v137
	ds_write2_b64 v90, v[86:87], v[88:89] offset0:136 offset1:170
	v_cvt_pk_f16_f32 v87, v142, v143
	v_cvt_pk_f16_f32 v86, v140, v141
	v_cvt_pk_f16_f32 v89, v146, v147
	v_cvt_pk_f16_f32 v88, v144, v145
	ds_write2_b64 v90, v[86:87], v[88:89] offset0:204 offset1:238
	v_fma_f32 v48, -v82, v84, 1.0
	v_fmac_f32_e32 v84, v48, v84
	v_mul_f32_e32 v48, v83, v84
	s_waitcnt lgkmcnt(11)
	v_mfma_f32_32x32x16_f16 v[16:31], v[32:35], v[58:61], v[16:31]
	s_waitcnt lgkmcnt(7)
	v_add_f32_e64 v32, v0, v40
	v_add_f32_e64 v33, v1, v41
	v_add_f32_e64 v0, v42, v2
	v_add_f32_e64 v1, v43, v3
	s_waitcnt lgkmcnt(6)
	v_pk_add_f32 v[2:3], v[4:5], v[44:45]
	v_pk_add_f32 v[4:5], v[46:47], v[6:7]
	s_waitcnt lgkmcnt(5)
	v_pk_add_f32 v[6:7], v[8:9], v[74:75]
	s_waitcnt lgkmcnt(4)
	v_pk_add_f32 v[8:9], v[12:13], v[78:79]
	v_fma_f32 v12, -v82, v48, v83
	v_mfma_f32_32x32x16_f16 v[16:31], v[36:39], v[62:65], v[16:31]
	v_fmac_f32_e32 v48, v12, v84
	v_cvt_pk_f16_f32 v2, v2, v3
	v_cvt_pk_f16_f32 v3, v4, v5
	v_cvt_pk_f16_f32 v1, v0, v1
	v_cvt_pk_f16_f32 v0, v32, v33
	v_fma_f32 v4, -v82, v48, v83
	v_div_fmas_f32 v4, v4, v84, v48
	v_mfma_f32_32x32x16_f16 v[16:31], v[50:53], v[66:69], v[16:31]
	v_add_f32_e64 v40, v76, v10
	v_add_f32_e64 v41, v77, v11
	v_add_f32_e64 v10, v80, v14
	v_add_f32_e64 v11, v81, v15
	v_div_fixup_f32 v4, v4, s10, 1.0
	v_cvt_pk_f16_f32 v34, v8, v9
	v_cvt_pk_f16_f32 v32, v6, v7
	v_cvt_pk_f16_f32 v35, v10, v11
	v_cvt_pk_f16_f32 v33, v40, v41
	v_mfma_f32_32x32x16_f16 v[16:31], v[54:57], v[70:73], v[16:31]
	s_andn2_b64 vcc, exec, s[8:9]
	s_nop 10
	v_mul_f32_e32 v8, v4, v16
	v_mul_f32_e32 v9, v4, v17
	v_mul_f32_e32 v5, v4, v18
	v_mul_f32_e32 v10, v4, v19
	v_mul_f32_e32 v6, v4, v20
	v_mul_f32_e32 v11, v4, v21
	v_mul_f32_e32 v7, v4, v22
	v_mul_f32_e32 v12, v4, v23
	v_mul_f32_e32 v16, v4, v24
	v_mul_f32_e32 v20, v4, v25
	v_mul_f32_e32 v17, v4, v26
	v_mul_f32_e32 v21, v4, v27
	v_mul_f32_e32 v18, v4, v28
	v_mul_f32_e32 v22, v4, v29
	v_mul_f32_e32 v19, v4, v30
	v_mul_f32_e32 v23, v4, v31
	v_cvt_pk_f16_f32 v7, v7, v12
	v_cvt_pk_f16_f32 v6, v6, v11
	v_cvt_pk_f16_f32 v5, v5, v10
	v_cvt_pk_f16_f32 v4, v8, v9
	v_cvt_pk_f16_f32 v19, v19, v23
	v_cvt_pk_f16_f32 v18, v18, v22
	v_mfma_f32_32x32x16_f16 v[0:15], v[0:3], v[4:7], 0
	v_cvt_pk_f16_f32 v17, v17, v21
	v_cvt_pk_f16_f32 v16, v16, v20
	s_nop 1
	v_mfma_f32_32x32x16_f16 v[0:15], v[32:35], v[16:19], v[0:15]
	s_cbranch_vccnz .LBB0_48
	v_lshlrev_b32_e32 v16, 7, v220
	v_lshl_or_b32 v16, v251, 12, v16
	v_mov_b32_e32 v17, v215
	s_add_i32 s33, s33, s46
	v_lshlrev_b32_e32 v22, 2, v214
	v_lshl_add_u64 v[16:17], v[16:17], 2, s[44:45]
	v_add_u32_e32 v18, s33, v214
	s_mov_b64 s[0:1], 0
	s_movk_i32 s10, 0x3fd
	v_mov_b32_e32 v23, v215
	s_branch .LBB0_43

.LBB0_48:
	s_nop 10
	v_cvt_pk_f16_f32 v7, v6, v7
	v_cvt_pk_f16_f32 v6, v4, v5
	v_cvt_pk_f16_f32 v4, v0, v1
	v_lshlrev_b32_e32 v0, 4, v218
	v_cvt_pk_f16_f32 v5, v2, v3
	v_lshl_or_b32 v16, v251, 11, v0
	v_cvt_pk_f16_f32 v3, v14, v15
	v_cvt_pk_f16_f32 v2, v12, v13
	v_cvt_pk_f16_f32 v1, v10, v11
	v_cvt_pk_f16_f32 v0, v8, v9
	ds_write_b128 v16, v[4:7] offset:43520
	ds_write_b128 v16, v[0:3] offset:44544
	s_branch .LBB0_49
.Lwos_nonworker:
	s_or_b64 exec, exec, s[6:7]
	ds_write2_b64 v76, v[72:73], v[74:75] offset1:34
	v_cvt_pk_f16_f32 v73, v126, v127
	v_cvt_pk_f16_f32 v72, v124, v125
	v_cvt_pk_f16_f32 v75, v130, v131
	v_cvt_pk_f16_f32 v74, v128, v129
	ds_write2_b64 v76, v[72:73], v[74:75] offset0:68 offset1:102
	v_cvt_pk_f16_f32 v73, v134, v135
	v_cvt_pk_f16_f32 v72, v132, v133
	v_cvt_pk_f16_f32 v75, v138, v139
	v_cvt_pk_f16_f32 v74, v136, v137
	ds_write2_b64 v76, v[72:73], v[74:75] offset0:136 offset1:170
	v_cvt_pk_f16_f32 v73, v142, v143
	v_cvt_pk_f16_f32 v72, v140, v141
	v_cvt_pk_f16_f32 v75, v146, v147
	v_cvt_pk_f16_f32 v74, v144, v145
	ds_write2_b64 v76, v[72:73], v[74:75] offset0:204 offset1:238
